# speedup vs baseline: 1.0272x; 1.0272x over previous
.LBB1_6:
	s_load_dwordx8 s[8:15], s[0:1], 0x10
	s_load_dwordx4 s[4:7], s[0:1], 0x30
	s_bfe_u32 s74, s2, 0x20003
	s_and_b64 vcc, exec, s[16:17]
	v_lshlrev_b32_e32 v34, 4, v34
	s_cbranch_vccz .LBB1_10
	s_load_dwordx4 s[16:19], s[0:1], 0x0
	s_lshl_b32 s24, s73, 22
	s_lshl_b32 s25, s74, 20
	s_or_b32 s38, s24, s25
	s_lshl_b32 s26, s72, 20
	s_lshl_b32 s27, s20, 12
	s_add_i32 s39, s27, 0xffff8000
	s_waitcnt lgkmcnt(0)
	s_add_u32 s16, s16, s26
	s_addc_u32 s17, s17, 0
	s_add_u32 s16, s16, s39
	s_addc_u32 s17, s17, 0
	s_add_u32 s18, s18, s38
	s_addc_u32 s19, s19, 0
	s_add_u32 s18, s18, s39
	s_addc_u32 s19, s19, 0
	s_add_u32 m0, s39, 0
	s_nop 0
	global_load_lds_dwordx4 v34, s[16:17]
	global_load_lds_dwordx4 v34, s[16:17] offset:1024
	global_load_lds_dwordx4 v34, s[16:17] offset:2048
	global_load_lds_dwordx4 v34, s[16:17] offset:3072
	s_add_u32 m0, s39, 16384
	s_add_u32 s16, s16, 0x4000
	s_addc_u32 s17, s17, 0
	global_load_lds_dwordx4 v34, s[18:19]
	global_load_lds_dwordx4 v34, s[18:19] offset:1024
	global_load_lds_dwordx4 v34, s[18:19] offset:2048
	global_load_lds_dwordx4 v34, s[18:19] offset:3072
	s_add_u32 s18, s18, 0x4000
	s_addc_u32 s19, s19, 0
	s_add_u32 m0, s39, 32768
	s_nop 0
	global_load_lds_dwordx4 v34, s[16:17]
	global_load_lds_dwordx4 v34, s[16:17] offset:1024
	global_load_lds_dwordx4 v34, s[16:17] offset:2048
	global_load_lds_dwordx4 v34, s[16:17] offset:3072
	s_add_u32 m0, s39, 49152
	s_add_u32 s16, s16, 0x4000
	s_addc_u32 s17, s17, 0
	global_load_lds_dwordx4 v34, s[18:19]
	global_load_lds_dwordx4 v34, s[18:19] offset:1024
	global_load_lds_dwordx4 v34, s[18:19] offset:2048
	global_load_lds_dwordx4 v34, s[18:19] offset:3072
	s_add_u32 s18, s18, 0x4000
	s_addc_u32 s19, s19, 0
	s_add_u32 m0, s39, 65536
	s_nop 0
	global_load_lds_dwordx4 v34, s[16:17]
	global_load_lds_dwordx4 v34, s[16:17] offset:1024
	global_load_lds_dwordx4 v34, s[16:17] offset:2048
	global_load_lds_dwordx4 v34, s[16:17] offset:3072
	s_add_u32 m0, s39, 81920
	s_add_u32 s16, s16, 0x4000
	s_addc_u32 s17, s17, 0
	global_load_lds_dwordx4 v34, s[18:19]
	global_load_lds_dwordx4 v34, s[18:19] offset:1024
	global_load_lds_dwordx4 v34, s[18:19] offset:2048
	global_load_lds_dwordx4 v34, s[18:19] offset:3072
	s_add_u32 s18, s18, 0x4000
	s_addc_u32 s19, s19, 0
	s_waitcnt vmcnt(16)
	s_barrier
	s_mov_b32 s41, 0
	s_add_u32 s40, s39, 0x18000
.Lq_ld_loop:
	s_mov_b32 m0, s40
	s_add_u32 s42, s40, 0x4000
	global_load_lds_dwordx4 v34, s[16:17]
	global_load_lds_dwordx4 v34, s[16:17] offset:1024
	global_load_lds_dwordx4 v34, s[16:17] offset:2048
	global_load_lds_dwordx4 v34, s[16:17] offset:3072
	s_mov_b32 m0, s42
	s_add_u32 s16, s16, 0x4000
	s_addc_u32 s17, s17, 0
	global_load_lds_dwordx4 v34, s[18:19]
	global_load_lds_dwordx4 v34, s[18:19] offset:1024
	global_load_lds_dwordx4 v34, s[18:19] offset:2048
	global_load_lds_dwordx4 v34, s[18:19] offset:3072
	s_add_u32 s18, s18, 0x4000
	s_addc_u32 s19, s19, 0
	s_add_u32 s40, s40, 0x8000
	s_and_b32 s40, s40, 0x1ffff
	s_waitcnt vmcnt(16)
	s_barrier
	s_add_u32 s41, s41, 1
	s_cmp_lt_u32 s41, 61
	s_cbranch_scc1 .Lq_ld_loop
	s_waitcnt vmcnt(8)
	s_barrier
	s_waitcnt vmcnt(0)
	s_barrier
	s_barrier
	s_barrier
	s_endpgm
